# P1 fp8 projection epilogue rope path: cs table loads for 4 row-groups prefetched ahead into spare VGPRs with counted vmcnt, redundant vmcnt(0) waits on store acks removed
# baseline (speedup 1.0000x reference)
.LBB0_375:
	s_lshl_b32 s4, s4, 8
	s_add_i32 s4, s4, s39
	v_and_or_b32 v16, v18, 15, s4
	s_and_b64 s[4:5], s[46:47], s[6:7]
	v_and_b32_e32 v0, 16, v18
	v_mov_b32_e32 v12, 0
	v_cndmask_b32_e64 v1, 0, 1, s[4:5]
	v_ashrrev_i32_e32 v17, 31, v16
	v_cmp_ne_u32_e64 s[6:7], 1, v1
	s_andn2_b64 vcc, exec, s[4:5]
	v_lshlrev_b32_e32 v168, 2, v0
	v_mov_b32_e32 v13, v12
	v_mov_b32_e32 v14, v12
	v_mov_b32_e32 v15, v12
	v_mov_b32_e32 v8, v12
	v_mov_b32_e32 v9, v12
	v_mov_b32_e32 v10, v12
	v_mov_b32_e32 v11, v12
	v_mov_b32_e32 v4, v12
	v_mov_b32_e32 v5, v12
	v_mov_b32_e32 v6, v12
	v_mov_b32_e32 v7, v12
	v_mov_b32_e32 v0, v12
	v_mov_b32_e32 v1, v12
	v_mov_b32_e32 v2, v12
	v_mov_b32_e32 v3, v12
	s_cbranch_vccnz .LBB0_377
	v_lshlrev_b64 v[238:239], 7, v[16:17]
	v_lshl_add_u64 v[238:239], s[28:29], 0, v[238:239]
	v_lshl_add_u64 v[238:239], v[238:239], 0, v[168:169]
	s_mov_b64 s[98:99], 0x1000
	global_load_dwordx4 v[200:203], v[238:239], off
	global_load_dwordx4 v[196:199], v[238:239], off offset:16
	global_load_dwordx4 v[192:195], v[238:239], off offset:32
	global_load_dwordx4 v[188:191], v[238:239], off offset:48
	global_load_dwordx4 v[216:219], v[238:239], off offset:2048
	global_load_dwordx4 v[212:215], v[238:239], off offset:2064
	global_load_dwordx4 v[208:211], v[238:239], off offset:2080
	global_load_dwordx4 v[204:207], v[238:239], off offset:2096
	v_lshl_add_u64 v[240:241], v[238:239], 0, s[98:99]
	global_load_dwordx4 v[234:237], v[240:241], off
	global_load_dwordx4 v[230:233], v[240:241], off offset:16
	global_load_dwordx4 v[226:229], v[240:241], off offset:32
	global_load_dwordx4 v[222:225], v[240:241], off offset:48
	global_load_dwordx4 v[12:15], v[240:241], off offset:2048
	global_load_dwordx4 v[8:11], v[240:241], off offset:2064
	global_load_dwordx4 v[4:7], v[240:241], off offset:2080
	global_load_dwordx4 v[0:3], v[240:241], off offset:2096
.LBB0_377:
	v_ashrrev_i32_e32 v18, 4, v18
	v_cmp_gt_i32_e64 s[4:5], 2, v18
	v_pk_mul_f32 v[22:23], v[158:159], s[48:49] op_sel_hi:[1,0]
	v_pk_mul_f32 v[24:25], v[156:157], s[48:49] op_sel_hi:[1,0]
	v_pk_mul_f32 v[26:27], v[154:155], s[48:49] op_sel_hi:[1,0]
	s_and_b64 vcc, exec, s[6:7]
	v_pk_mul_f32 v[28:29], v[152:153], s[48:49] op_sel_hi:[1,0]
	s_cbranch_vccnz .LBB0_458
	v_and_b32_e32 v20, 64, v186
	v_xor_b32_e32 v19, 32, v186
	v_add_u32_e32 v20, 64, v20
	v_cmp_lt_i32_e32 vcc, v19, v20
	s_waitcnt vmcnt(12)
	v_mov_b32_e32 v174, v201
	v_mov_b32_e32 v175, v203
	v_cndmask_b32_e32 v19, v186, v19, vcc
	v_lshlrev_b32_e32 v19, 2, v19
	ds_bpermute_b32 v20, v19, v24
	ds_bpermute_b32 v21, v19, v25
	v_mov_b32_e32 v30, v200
	v_mov_b32_e32 v31, v202
	s_waitcnt lgkmcnt(0)
	v_pk_mul_f32 v[20:21], v[174:175], v[20:21]
	s_nop 0
	v_cndmask_b32_e64 v21, v21, -v21, s[4:5]
	v_cndmask_b32_e64 v20, v20, -v20, s[4:5]
	v_pk_fma_f32 v[24:25], v[24:25], v[30:31], v[20:21]
	ds_bpermute_b32 v20, v19, v22
	ds_bpermute_b32 v21, v19, v23
	v_mov_b32_e32 v174, v197
	v_mov_b32_e32 v175, v199
	v_mov_b32_e32 v30, v196
	v_mov_b32_e32 v31, v198
	s_waitcnt lgkmcnt(0)
	v_pk_mul_f32 v[20:21], v[174:175], v[20:21]
	v_mov_b32_e32 v174, v193
	v_cndmask_b32_e64 v21, v21, -v21, s[4:5]
	v_cndmask_b32_e64 v20, v20, -v20, s[4:5]
	v_pk_fma_f32 v[22:23], v[22:23], v[30:31], v[20:21]
	ds_bpermute_b32 v20, v19, v28
	ds_bpermute_b32 v21, v19, v29
	v_mov_b32_e32 v175, v195
	v_mov_b32_e32 v30, v192
	v_mov_b32_e32 v31, v194
	s_waitcnt lgkmcnt(0)
	v_pk_mul_f32 v[20:21], v[174:175], v[20:21]
	s_nop 0
	v_cndmask_b32_e64 v21, v21, -v21, s[4:5]
	v_cndmask_b32_e64 v20, v20, -v20, s[4:5]
	v_pk_fma_f32 v[28:29], v[28:29], v[30:31], v[20:21]
	ds_bpermute_b32 v20, v19, v26
	ds_bpermute_b32 v21, v19, v27
	v_mov_b32_e32 v174, v189
	v_mov_b32_e32 v175, v191
	v_mov_b32_e32 v30, v188
	v_mov_b32_e32 v31, v190
	s_waitcnt lgkmcnt(0)
	v_pk_mul_f32 v[20:21], v[174:175], v[20:21]
	s_nop 0
	v_cndmask_b32_e64 v21, v21, -v21, s[4:5]
	v_cndmask_b32_e64 v20, v20, -v20, s[4:5]
	v_pk_fma_f32 v[26:27], v[26:27], v[30:31], v[20:21]
	v_cndmask_b32_e64 v19, 0, 1, s[10:11]
	v_cmp_ne_u32_e64 s[8:9], 1, v19
	s_andn2_b64 vcc, exec, s[10:11]
	s_cbranch_vccz .LBB0_459

.LBB0_381:
	s_add_i32 s30, s30, s49
	v_lshl_add_u32 v18, v18, 3, s30
	v_ashrrev_i32_e32 v19, 31, v18
	v_mul_lo_u32 v30, s75, v16
	v_mul_lo_u32 v17, s74, v17
	v_mad_u64_u32 v[20:21], s[30:31], s74, v16, 0
	v_lshl_add_u64 v[18:19], v[18:19], 1, s[76:77]
	v_add3_u32 v21, v21, v17, v30
	v_lshl_add_u64 v[20:21], v[20:21], 1, v[18:19]
	v_cvt_pk_bf16_f32 v152, v24, v25
	v_cvt_pk_bf16_f32 v153, v22, v23
	v_cvt_pk_bf16_f32 v154, v28, v29
	v_cvt_pk_bf16_f32 v155, v26, v27
	v_pk_mul_f32 v[22:23], v[150:151], s[48:49] op_sel_hi:[1,0]
	v_pk_mul_f32 v[24:25], v[148:149], s[48:49] op_sel_hi:[1,0]
	v_pk_mul_f32 v[26:27], v[146:147], s[48:49] op_sel_hi:[1,0]
	s_and_b64 vcc, exec, s[6:7]
	v_pk_mul_f32 v[28:29], v[144:145], s[48:49] op_sel_hi:[1,0]
	global_store_dwordx4 v[20:21], v[152:155], off
	s_cbranch_vccnz .LBB0_460
	v_and_b32_e32 v30, 64, v186
	v_xor_b32_e32 v17, 32, v186
	v_add_u32_e32 v30, 64, v30
	v_cmp_lt_i32_e32 vcc, v17, v30
	v_mov_b32_e32 v154, v201
	v_mov_b32_e32 v155, v203
	v_cndmask_b32_e32 v17, v186, v17, vcc
	v_lshlrev_b32_e32 v17, 2, v17
	ds_bpermute_b32 v30, v17, v24
	ds_bpermute_b32 v31, v17, v25
	v_mov_b32_e32 v152, v200
	v_mov_b32_e32 v153, v202
	s_waitcnt lgkmcnt(0)
	v_pk_mul_f32 v[30:31], v[154:155], v[30:31]
	s_nop 0
	v_cndmask_b32_e64 v31, v31, -v31, s[4:5]
	v_cndmask_b32_e64 v30, v30, -v30, s[4:5]
	v_pk_fma_f32 v[24:25], v[24:25], v[152:153], v[30:31]
	ds_bpermute_b32 v30, v17, v22
	ds_bpermute_b32 v31, v17, v23
	v_mov_b32_e32 v154, v197
	v_mov_b32_e32 v155, v199
	v_mov_b32_e32 v152, v196
	v_mov_b32_e32 v153, v198
	s_waitcnt lgkmcnt(0)
	v_pk_mul_f32 v[30:31], v[154:155], v[30:31]
	v_mov_b32_e32 v154, v193
	v_cndmask_b32_e64 v31, v31, -v31, s[4:5]
	v_cndmask_b32_e64 v30, v30, -v30, s[4:5]
	v_pk_fma_f32 v[22:23], v[22:23], v[152:153], v[30:31]
	ds_bpermute_b32 v30, v17, v28
	ds_bpermute_b32 v31, v17, v29
	v_mov_b32_e32 v155, v195
	v_mov_b32_e32 v152, v192
	v_mov_b32_e32 v153, v194
	s_waitcnt lgkmcnt(0)
	v_pk_mul_f32 v[30:31], v[154:155], v[30:31]
	s_nop 0
	v_cndmask_b32_e64 v31, v31, -v31, s[4:5]
	v_cndmask_b32_e64 v30, v30, -v30, s[4:5]
	v_pk_fma_f32 v[28:29], v[28:29], v[152:153], v[30:31]
	ds_bpermute_b32 v30, v17, v26
	ds_bpermute_b32 v31, v17, v27
	v_mov_b32_e32 v154, v189
	v_mov_b32_e32 v155, v191
	v_mov_b32_e32 v152, v188
	v_mov_b32_e32 v153, v190
	s_waitcnt lgkmcnt(0)
	v_pk_mul_f32 v[30:31], v[154:155], v[30:31]
	s_nop 0
	v_cndmask_b32_e64 v31, v31, -v31, s[4:5]
	v_cndmask_b32_e64 v30, v30, -v30, s[4:5]
	v_pk_fma_f32 v[26:27], v[26:27], v[152:153], v[30:31]
	s_and_b64 vcc, exec, s[8:9]
	s_cbranch_vccz .LBB0_461

.LBB0_385:
	v_cvt_pk_bf16_f32 v144, v24, v25
	v_cvt_pk_bf16_f32 v145, v22, v23
	v_cvt_pk_bf16_f32 v146, v28, v29
	v_cvt_pk_bf16_f32 v147, v26, v27
	global_store_dwordx4 v[20:21], v[144:147], off offset:256
	v_or_b32_e32 v20, 16, v16
	s_and_b64 vcc, exec, s[6:7]
	v_ashrrev_i32_e32 v21, 31, v20
	s_cbranch_vccnz .LBB0_387
	s_mov_b64 s[98:99], 0x4000
	v_lshl_add_u64 v[240:241], v[238:239], 0, s[98:99]
	global_load_dwordx4 v[200:203], v[240:241], off
	global_load_dwordx4 v[196:199], v[240:241], off offset:16
	global_load_dwordx4 v[192:195], v[240:241], off offset:32
	global_load_dwordx4 v[188:191], v[240:241], off offset:48
.LBB0_387:
	v_pk_mul_f32 v[22:23], v[142:143], s[48:49] op_sel_hi:[1,0]
	v_pk_mul_f32 v[24:25], v[140:141], s[48:49] op_sel_hi:[1,0]
	v_pk_mul_f32 v[26:27], v[138:139], s[48:49] op_sel_hi:[1,0]
	s_and_b64 vcc, exec, s[6:7]
	v_pk_mul_f32 v[28:29], v[136:137], s[48:49] op_sel_hi:[1,0]
	s_cbranch_vccnz .LBB0_462
	v_and_b32_e32 v30, 64, v186
	v_xor_b32_e32 v17, 32, v186
	v_add_u32_e32 v30, 64, v30
	v_cmp_lt_i32_e32 vcc, v17, v30
	s_waitcnt vmcnt(14)
	v_mov_b32_e32 v146, v217
	v_mov_b32_e32 v147, v219
	v_cndmask_b32_e32 v17, v186, v17, vcc
	v_lshlrev_b32_e32 v17, 2, v17
	ds_bpermute_b32 v30, v17, v24
	ds_bpermute_b32 v31, v17, v25
	v_mov_b32_e32 v144, v216
	v_mov_b32_e32 v145, v218
	s_waitcnt lgkmcnt(0)
	v_pk_mul_f32 v[30:31], v[146:147], v[30:31]
	s_nop 0
	v_cndmask_b32_e64 v31, v31, -v31, s[4:5]
	v_cndmask_b32_e64 v30, v30, -v30, s[4:5]
	v_pk_fma_f32 v[24:25], v[24:25], v[144:145], v[30:31]
	ds_bpermute_b32 v30, v17, v22
	ds_bpermute_b32 v31, v17, v23
	v_mov_b32_e32 v146, v213
	v_mov_b32_e32 v147, v215
	v_mov_b32_e32 v144, v212
	v_mov_b32_e32 v145, v214
	s_waitcnt lgkmcnt(0)
	v_pk_mul_f32 v[30:31], v[146:147], v[30:31]
	v_mov_b32_e32 v146, v209
	v_cndmask_b32_e64 v31, v31, -v31, s[4:5]
	v_cndmask_b32_e64 v30, v30, -v30, s[4:5]
	v_pk_fma_f32 v[22:23], v[22:23], v[144:145], v[30:31]
	ds_bpermute_b32 v30, v17, v28
	ds_bpermute_b32 v31, v17, v29
	v_mov_b32_e32 v147, v211
	v_mov_b32_e32 v144, v208
	v_mov_b32_e32 v145, v210
	s_waitcnt lgkmcnt(0)
	v_pk_mul_f32 v[30:31], v[146:147], v[30:31]
	s_nop 0
	v_cndmask_b32_e64 v31, v31, -v31, s[4:5]
	v_cndmask_b32_e64 v30, v30, -v30, s[4:5]
	v_pk_fma_f32 v[28:29], v[28:29], v[144:145], v[30:31]
	ds_bpermute_b32 v30, v17, v26
	ds_bpermute_b32 v31, v17, v27
	v_mov_b32_e32 v146, v205
	v_mov_b32_e32 v147, v207
	v_mov_b32_e32 v144, v204
	v_mov_b32_e32 v145, v206
	s_waitcnt lgkmcnt(0)
	v_pk_mul_f32 v[30:31], v[146:147], v[30:31]
	s_nop 0
	v_cndmask_b32_e64 v31, v31, -v31, s[4:5]
	v_cndmask_b32_e64 v30, v30, -v30, s[4:5]
	v_pk_fma_f32 v[26:27], v[26:27], v[144:145], v[30:31]
	s_and_b64 vcc, exec, s[8:9]
	s_cbranch_vccz .LBB0_463

.LBB0_391:
	v_mul_lo_u32 v17, s75, v20
	v_mul_lo_u32 v30, s74, v21
	v_mad_u64_u32 v[20:21], s[30:31], s74, v20, 0
	v_add3_u32 v21, v21, v30, v17
	v_lshl_add_u64 v[20:21], v[20:21], 1, v[18:19]
	v_cvt_pk_bf16_f32 v136, v24, v25
	v_cvt_pk_bf16_f32 v137, v22, v23
	v_cvt_pk_bf16_f32 v138, v28, v29
	v_cvt_pk_bf16_f32 v139, v26, v27
	v_pk_mul_f32 v[22:23], v[134:135], s[48:49] op_sel_hi:[1,0]
	v_pk_mul_f32 v[24:25], v[132:133], s[48:49] op_sel_hi:[1,0]
	v_pk_mul_f32 v[26:27], v[130:131], s[48:49] op_sel_hi:[1,0]
	s_and_b64 vcc, exec, s[6:7]
	v_pk_mul_f32 v[28:29], v[128:129], s[48:49] op_sel_hi:[1,0]
	global_store_dwordx4 v[20:21], v[136:139], off
	s_cbranch_vccnz .LBB0_464
	v_and_b32_e32 v30, 64, v186
	v_xor_b32_e32 v17, 32, v186
	v_add_u32_e32 v30, 64, v30
	v_cmp_lt_i32_e32 vcc, v17, v30
	v_mov_b32_e32 v138, v217
	v_mov_b32_e32 v139, v219
	v_cndmask_b32_e32 v17, v186, v17, vcc
	v_lshlrev_b32_e32 v17, 2, v17
	ds_bpermute_b32 v30, v17, v24
	ds_bpermute_b32 v31, v17, v25
	v_mov_b32_e32 v136, v216
	v_mov_b32_e32 v137, v218
	s_waitcnt lgkmcnt(0)
	v_pk_mul_f32 v[30:31], v[138:139], v[30:31]
	s_nop 0
	v_cndmask_b32_e64 v31, v31, -v31, s[4:5]
	v_cndmask_b32_e64 v30, v30, -v30, s[4:5]
	v_pk_fma_f32 v[24:25], v[24:25], v[136:137], v[30:31]
	ds_bpermute_b32 v30, v17, v22
	ds_bpermute_b32 v31, v17, v23
	v_mov_b32_e32 v138, v213
	v_mov_b32_e32 v139, v215
	v_mov_b32_e32 v136, v212
	v_mov_b32_e32 v137, v214
	s_waitcnt lgkmcnt(0)
	v_pk_mul_f32 v[30:31], v[138:139], v[30:31]
	v_mov_b32_e32 v138, v209
	v_cndmask_b32_e64 v31, v31, -v31, s[4:5]
	v_cndmask_b32_e64 v30, v30, -v30, s[4:5]
	v_pk_fma_f32 v[22:23], v[22:23], v[136:137], v[30:31]
	ds_bpermute_b32 v30, v17, v28
	ds_bpermute_b32 v31, v17, v29
	v_mov_b32_e32 v139, v211
	v_mov_b32_e32 v136, v208
	v_mov_b32_e32 v137, v210
	s_waitcnt lgkmcnt(0)
	v_pk_mul_f32 v[30:31], v[138:139], v[30:31]
	s_nop 0
	v_cndmask_b32_e64 v31, v31, -v31, s[4:5]
	v_cndmask_b32_e64 v30, v30, -v30, s[4:5]
	v_pk_fma_f32 v[28:29], v[28:29], v[136:137], v[30:31]
	ds_bpermute_b32 v30, v17, v26
	ds_bpermute_b32 v31, v17, v27
	v_mov_b32_e32 v138, v205
	v_mov_b32_e32 v139, v207
	v_mov_b32_e32 v136, v204
	v_mov_b32_e32 v137, v206
	s_waitcnt lgkmcnt(0)
	v_pk_mul_f32 v[30:31], v[138:139], v[30:31]
	s_nop 0
	v_cndmask_b32_e64 v31, v31, -v31, s[4:5]
	v_cndmask_b32_e64 v30, v30, -v30, s[4:5]
	v_pk_fma_f32 v[26:27], v[26:27], v[136:137], v[30:31]
	s_and_b64 vcc, exec, s[8:9]
	s_cbranch_vccz .LBB0_465

.LBB0_395:
	v_cvt_pk_bf16_f32 v128, v24, v25
	v_cvt_pk_bf16_f32 v129, v22, v23
	v_cvt_pk_bf16_f32 v130, v28, v29
	v_cvt_pk_bf16_f32 v131, v26, v27
	global_store_dwordx4 v[20:21], v[128:131], off offset:256
	v_or_b32_e32 v20, 32, v16
	s_and_b64 vcc, exec, s[6:7]
	v_ashrrev_i32_e32 v21, 31, v20
	s_cbranch_vccnz .LBB0_397
	global_load_dwordx4 v[216:219], v[240:241], off offset:2048
	global_load_dwordx4 v[212:215], v[240:241], off offset:2064
	global_load_dwordx4 v[208:211], v[240:241], off offset:2080
	global_load_dwordx4 v[204:207], v[240:241], off offset:2096
.LBB0_397:
	v_pk_mul_f32 v[22:23], v[126:127], s[48:49] op_sel_hi:[1,0]
	v_pk_mul_f32 v[24:25], v[124:125], s[48:49] op_sel_hi:[1,0]
	v_pk_mul_f32 v[26:27], v[122:123], s[48:49] op_sel_hi:[1,0]
	s_and_b64 vcc, exec, s[6:7]
	v_pk_mul_f32 v[28:29], v[120:121], s[48:49] op_sel_hi:[1,0]
	s_cbranch_vccnz .LBB0_466
	v_and_b32_e32 v30, 64, v186
	v_xor_b32_e32 v17, 32, v186
	v_add_u32_e32 v30, 64, v30
	v_cmp_lt_i32_e32 vcc, v17, v30
	s_waitcnt vmcnt(16)
	v_mov_b32_e32 v130, v235
	v_mov_b32_e32 v131, v237
	v_cndmask_b32_e32 v17, v186, v17, vcc
	v_lshlrev_b32_e32 v17, 2, v17
	ds_bpermute_b32 v30, v17, v24
	ds_bpermute_b32 v31, v17, v25
	v_mov_b32_e32 v128, v234
	v_mov_b32_e32 v129, v236
	s_waitcnt lgkmcnt(0)
	v_pk_mul_f32 v[30:31], v[130:131], v[30:31]
	s_nop 0
	v_cndmask_b32_e64 v31, v31, -v31, s[4:5]
	v_cndmask_b32_e64 v30, v30, -v30, s[4:5]
	v_pk_fma_f32 v[24:25], v[24:25], v[128:129], v[30:31]
	ds_bpermute_b32 v30, v17, v22
	ds_bpermute_b32 v31, v17, v23
	v_mov_b32_e32 v130, v231
	v_mov_b32_e32 v131, v233
	v_mov_b32_e32 v128, v230
	v_mov_b32_e32 v129, v232
	s_waitcnt lgkmcnt(0)
	v_pk_mul_f32 v[30:31], v[130:131], v[30:31]
	v_mov_b32_e32 v130, v227
	v_cndmask_b32_e64 v31, v31, -v31, s[4:5]
	v_cndmask_b32_e64 v30, v30, -v30, s[4:5]
	v_pk_fma_f32 v[22:23], v[22:23], v[128:129], v[30:31]
	ds_bpermute_b32 v30, v17, v28
	ds_bpermute_b32 v31, v17, v29
	v_mov_b32_e32 v131, v229
	v_mov_b32_e32 v128, v226
	v_mov_b32_e32 v129, v228
	s_waitcnt lgkmcnt(0)
	v_pk_mul_f32 v[30:31], v[130:131], v[30:31]
	s_nop 0
	v_cndmask_b32_e64 v31, v31, -v31, s[4:5]
	v_cndmask_b32_e64 v30, v30, -v30, s[4:5]
	v_pk_fma_f32 v[28:29], v[28:29], v[128:129], v[30:31]
	ds_bpermute_b32 v30, v17, v26
	ds_bpermute_b32 v31, v17, v27
	v_mov_b32_e32 v130, v223
	v_mov_b32_e32 v131, v225
	v_mov_b32_e32 v128, v222
	v_mov_b32_e32 v129, v224
	s_waitcnt lgkmcnt(0)
	v_pk_mul_f32 v[30:31], v[130:131], v[30:31]
	s_nop 0
	v_cndmask_b32_e64 v31, v31, -v31, s[4:5]
	v_cndmask_b32_e64 v30, v30, -v30, s[4:5]
	v_pk_fma_f32 v[26:27], v[26:27], v[128:129], v[30:31]
	s_and_b64 vcc, exec, s[8:9]
	s_cbranch_vccz .LBB0_467

.LBB0_401:
	v_mul_lo_u32 v17, s75, v20
	v_mul_lo_u32 v30, s74, v21
	v_mad_u64_u32 v[20:21], s[30:31], s74, v20, 0
	v_add3_u32 v21, v21, v30, v17
	v_lshl_add_u64 v[20:21], v[20:21], 1, v[18:19]
	v_cvt_pk_bf16_f32 v120, v24, v25
	v_cvt_pk_bf16_f32 v121, v22, v23
	v_cvt_pk_bf16_f32 v122, v28, v29
	v_cvt_pk_bf16_f32 v123, v26, v27
	v_pk_mul_f32 v[22:23], v[118:119], s[48:49] op_sel_hi:[1,0]
	v_pk_mul_f32 v[24:25], v[116:117], s[48:49] op_sel_hi:[1,0]
	v_pk_mul_f32 v[26:27], v[114:115], s[48:49] op_sel_hi:[1,0]
	s_and_b64 vcc, exec, s[6:7]
	v_pk_mul_f32 v[28:29], v[112:113], s[48:49] op_sel_hi:[1,0]
	global_store_dwordx4 v[20:21], v[120:123], off
	s_cbranch_vccnz .LBB0_468
	v_and_b32_e32 v30, 64, v186
	v_xor_b32_e32 v17, 32, v186
	v_add_u32_e32 v30, 64, v30
	v_cmp_lt_i32_e32 vcc, v17, v30
	v_mov_b32_e32 v122, v235
	v_mov_b32_e32 v123, v237
	v_cndmask_b32_e32 v17, v186, v17, vcc
	v_lshlrev_b32_e32 v17, 2, v17
	ds_bpermute_b32 v30, v17, v24
	ds_bpermute_b32 v31, v17, v25
	v_mov_b32_e32 v120, v234
	v_mov_b32_e32 v121, v236
	s_waitcnt lgkmcnt(0)
	v_pk_mul_f32 v[30:31], v[122:123], v[30:31]
	s_nop 0
	v_cndmask_b32_e64 v31, v31, -v31, s[4:5]
	v_cndmask_b32_e64 v30, v30, -v30, s[4:5]
	v_pk_fma_f32 v[24:25], v[24:25], v[120:121], v[30:31]
	ds_bpermute_b32 v30, v17, v22
	ds_bpermute_b32 v31, v17, v23
	v_mov_b32_e32 v122, v231
	v_mov_b32_e32 v123, v233
	v_mov_b32_e32 v120, v230
	v_mov_b32_e32 v121, v232
	s_waitcnt lgkmcnt(0)
	v_pk_mul_f32 v[30:31], v[122:123], v[30:31]
	v_mov_b32_e32 v122, v227
	v_cndmask_b32_e64 v31, v31, -v31, s[4:5]
	v_cndmask_b32_e64 v30, v30, -v30, s[4:5]
	v_pk_fma_f32 v[22:23], v[22:23], v[120:121], v[30:31]
	ds_bpermute_b32 v30, v17, v28
	ds_bpermute_b32 v31, v17, v29
	v_mov_b32_e32 v123, v229
	v_mov_b32_e32 v120, v226
	v_mov_b32_e32 v121, v228
	s_waitcnt lgkmcnt(0)
	v_pk_mul_f32 v[30:31], v[122:123], v[30:31]
	s_nop 0
	v_cndmask_b32_e64 v31, v31, -v31, s[4:5]
	v_cndmask_b32_e64 v30, v30, -v30, s[4:5]
	v_pk_fma_f32 v[28:29], v[28:29], v[120:121], v[30:31]
	ds_bpermute_b32 v30, v17, v26
	ds_bpermute_b32 v31, v17, v27
	v_mov_b32_e32 v122, v223
	v_mov_b32_e32 v123, v225
	v_mov_b32_e32 v120, v222
	v_mov_b32_e32 v121, v224
	s_waitcnt lgkmcnt(0)
	v_pk_mul_f32 v[30:31], v[122:123], v[30:31]
	s_nop 0
	v_cndmask_b32_e64 v31, v31, -v31, s[4:5]
	v_cndmask_b32_e64 v30, v30, -v30, s[4:5]
	v_pk_fma_f32 v[26:27], v[26:27], v[120:121], v[30:31]
	s_and_b64 vcc, exec, s[8:9]
	s_cbranch_vccz .LBB0_469

.LBB0_405:
	v_cvt_pk_bf16_f32 v112, v24, v25
	v_cvt_pk_bf16_f32 v113, v22, v23
	v_cvt_pk_bf16_f32 v114, v28, v29
	v_cvt_pk_bf16_f32 v115, v26, v27
	global_store_dwordx4 v[20:21], v[112:115], off offset:256
	v_or_b32_e32 v20, 48, v16
	s_and_b64 vcc, exec, s[6:7]
	v_ashrrev_i32_e32 v21, 31, v20
	s_cbranch_vccnz .LBB0_407
	s_mov_b64 s[98:99], 0x5000
	v_lshl_add_u64 v[240:241], v[238:239], 0, s[98:99]
	global_load_dwordx4 v[234:237], v[240:241], off
	global_load_dwordx4 v[230:233], v[240:241], off offset:16
	global_load_dwordx4 v[226:229], v[240:241], off offset:32
	global_load_dwordx4 v[222:225], v[240:241], off offset:48
.LBB0_407:
	v_pk_mul_f32 v[22:23], v[110:111], s[48:49] op_sel_hi:[1,0]
	v_pk_mul_f32 v[24:25], v[108:109], s[48:49] op_sel_hi:[1,0]
	v_pk_mul_f32 v[26:27], v[106:107], s[48:49] op_sel_hi:[1,0]
	s_and_b64 vcc, exec, s[6:7]
	v_pk_mul_f32 v[28:29], v[104:105], s[48:49] op_sel_hi:[1,0]
	s_cbranch_vccnz .LBB0_470
	v_and_b32_e32 v30, 64, v186
	v_xor_b32_e32 v17, 32, v186
	v_add_u32_e32 v30, 64, v30
	v_cmp_lt_i32_e32 vcc, v17, v30
	s_waitcnt vmcnt(18)
	v_mov_b32_e32 v114, v13
	v_mov_b32_e32 v115, v15
	v_cndmask_b32_e32 v17, v186, v17, vcc
	v_lshlrev_b32_e32 v17, 2, v17
	ds_bpermute_b32 v30, v17, v24
	ds_bpermute_b32 v31, v17, v25
	v_mov_b32_e32 v112, v12
	v_mov_b32_e32 v113, v14
	s_waitcnt lgkmcnt(0)
	v_pk_mul_f32 v[30:31], v[114:115], v[30:31]
	s_nop 0
	v_cndmask_b32_e64 v31, v31, -v31, s[4:5]
	v_cndmask_b32_e64 v30, v30, -v30, s[4:5]
	v_pk_fma_f32 v[24:25], v[24:25], v[112:113], v[30:31]
	ds_bpermute_b32 v30, v17, v22
	ds_bpermute_b32 v31, v17, v23
	v_mov_b32_e32 v114, v9
	v_mov_b32_e32 v115, v11
	v_mov_b32_e32 v112, v8
	v_mov_b32_e32 v113, v10
	s_waitcnt lgkmcnt(0)
	v_pk_mul_f32 v[30:31], v[114:115], v[30:31]
	v_mov_b32_e32 v114, v5
	v_cndmask_b32_e64 v31, v31, -v31, s[4:5]
	v_cndmask_b32_e64 v30, v30, -v30, s[4:5]
	v_pk_fma_f32 v[22:23], v[22:23], v[112:113], v[30:31]
	ds_bpermute_b32 v30, v17, v28
	ds_bpermute_b32 v31, v17, v29
	v_mov_b32_e32 v115, v7
	v_mov_b32_e32 v112, v4
	v_mov_b32_e32 v113, v6
	s_waitcnt lgkmcnt(0)
	v_pk_mul_f32 v[30:31], v[114:115], v[30:31]
	s_nop 0
	v_cndmask_b32_e64 v31, v31, -v31, s[4:5]
	v_cndmask_b32_e64 v30, v30, -v30, s[4:5]
	v_pk_fma_f32 v[28:29], v[28:29], v[112:113], v[30:31]
	ds_bpermute_b32 v30, v17, v26
	ds_bpermute_b32 v31, v17, v27
	v_mov_b32_e32 v114, v1
	v_mov_b32_e32 v115, v3
	v_mov_b32_e32 v112, v0
	v_mov_b32_e32 v113, v2
	s_waitcnt lgkmcnt(0)
	v_pk_mul_f32 v[30:31], v[114:115], v[30:31]
	s_nop 0
	v_cndmask_b32_e64 v31, v31, -v31, s[4:5]
	v_cndmask_b32_e64 v30, v30, -v30, s[4:5]
	v_pk_fma_f32 v[26:27], v[26:27], v[112:113], v[30:31]
	s_and_b64 vcc, exec, s[8:9]
	s_cbranch_vccz .LBB0_471

.LBB0_411:
	v_mul_lo_u32 v17, s75, v20
	v_mul_lo_u32 v30, s74, v21
	v_mad_u64_u32 v[20:21], s[30:31], s74, v20, 0
	v_add3_u32 v21, v21, v30, v17
	v_lshl_add_u64 v[20:21], v[20:21], 1, v[18:19]
	v_cvt_pk_bf16_f32 v104, v24, v25
	v_cvt_pk_bf16_f32 v105, v22, v23
	v_cvt_pk_bf16_f32 v106, v28, v29
	v_cvt_pk_bf16_f32 v107, v26, v27
	v_pk_mul_f32 v[22:23], v[102:103], s[48:49] op_sel_hi:[1,0]
	v_pk_mul_f32 v[24:25], v[100:101], s[48:49] op_sel_hi:[1,0]
	v_pk_mul_f32 v[26:27], v[98:99], s[48:49] op_sel_hi:[1,0]
	s_and_b64 vcc, exec, s[6:7]
	v_pk_mul_f32 v[28:29], v[96:97], s[48:49] op_sel_hi:[1,0]
	global_store_dwordx4 v[20:21], v[104:107], off
	s_cbranch_vccnz .LBB0_472
	v_and_b32_e32 v30, 64, v186
	v_xor_b32_e32 v17, 32, v186
	v_add_u32_e32 v30, 64, v30
	v_cmp_lt_i32_e32 vcc, v17, v30
	v_mov_b32_e32 v106, v13
	v_mov_b32_e32 v107, v15
	v_cndmask_b32_e32 v17, v186, v17, vcc
	v_lshlrev_b32_e32 v17, 2, v17
	ds_bpermute_b32 v30, v17, v24
	ds_bpermute_b32 v31, v17, v25
	v_mov_b32_e32 v104, v12
	v_mov_b32_e32 v105, v14
	s_waitcnt lgkmcnt(0)
	v_pk_mul_f32 v[30:31], v[106:107], v[30:31]
	s_nop 0
	v_cndmask_b32_e64 v31, v31, -v31, s[4:5]
	v_cndmask_b32_e64 v30, v30, -v30, s[4:5]
	v_pk_fma_f32 v[24:25], v[24:25], v[104:105], v[30:31]
	ds_bpermute_b32 v30, v17, v22
	ds_bpermute_b32 v31, v17, v23
	v_mov_b32_e32 v106, v9
	v_mov_b32_e32 v107, v11
	v_mov_b32_e32 v104, v8
	v_mov_b32_e32 v105, v10
	s_waitcnt lgkmcnt(0)
	v_pk_mul_f32 v[30:31], v[106:107], v[30:31]
	v_mov_b32_e32 v106, v5
	v_cndmask_b32_e64 v31, v31, -v31, s[4:5]
	v_cndmask_b32_e64 v30, v30, -v30, s[4:5]
	v_pk_fma_f32 v[22:23], v[22:23], v[104:105], v[30:31]
	ds_bpermute_b32 v30, v17, v28
	ds_bpermute_b32 v31, v17, v29
	v_mov_b32_e32 v107, v7
	v_mov_b32_e32 v104, v4
	v_mov_b32_e32 v105, v6
	s_waitcnt lgkmcnt(0)
	v_pk_mul_f32 v[30:31], v[106:107], v[30:31]
	s_nop 0
	v_cndmask_b32_e64 v31, v31, -v31, s[4:5]
	v_cndmask_b32_e64 v30, v30, -v30, s[4:5]
	v_pk_fma_f32 v[28:29], v[28:29], v[104:105], v[30:31]
	ds_bpermute_b32 v30, v17, v26
	ds_bpermute_b32 v31, v17, v27
	v_mov_b32_e32 v106, v1
	v_mov_b32_e32 v107, v3
	v_mov_b32_e32 v104, v0
	v_mov_b32_e32 v105, v2
	s_waitcnt lgkmcnt(0)
	v_pk_mul_f32 v[30:31], v[106:107], v[30:31]
	s_nop 0
	v_cndmask_b32_e64 v31, v31, -v31, s[4:5]
	v_cndmask_b32_e64 v30, v30, -v30, s[4:5]
	v_pk_fma_f32 v[26:27], v[26:27], v[104:105], v[30:31]
	s_and_b64 vcc, exec, s[8:9]
	s_cbranch_vccz .LBB0_473

.LBB0_415:
	v_cvt_pk_bf16_f32 v96, v24, v25
	v_cvt_pk_bf16_f32 v97, v22, v23
	v_cvt_pk_bf16_f32 v98, v28, v29
	v_cvt_pk_bf16_f32 v99, v26, v27
	global_store_dwordx4 v[20:21], v[96:99], off offset:256
	v_add_u32_e32 v20, 0x80, v16
	s_and_b64 vcc, exec, s[6:7]
	v_ashrrev_i32_e32 v21, 31, v20
	s_cbranch_vccnz .LBB0_417
	global_load_dwordx4 v[12:15], v[240:241], off offset:2048
	global_load_dwordx4 v[8:11], v[240:241], off offset:2064
	global_load_dwordx4 v[4:7], v[240:241], off offset:2080
	global_load_dwordx4 v[0:3], v[240:241], off offset:2096
.LBB0_417:
	v_pk_mul_f32 v[22:23], v[94:95], s[48:49] op_sel_hi:[1,0]
	v_pk_mul_f32 v[24:25], v[92:93], s[48:49] op_sel_hi:[1,0]
	v_pk_mul_f32 v[26:27], v[90:91], s[48:49] op_sel_hi:[1,0]
	s_and_b64 vcc, exec, s[6:7]
	v_pk_mul_f32 v[28:29], v[88:89], s[48:49] op_sel_hi:[1,0]
	s_cbranch_vccnz .LBB0_474
	v_and_b32_e32 v30, 64, v186
	v_xor_b32_e32 v17, 32, v186
	v_add_u32_e32 v30, 64, v30
	v_cmp_lt_i32_e32 vcc, v17, v30
	s_waitcnt vmcnt(18)
	v_mov_b32_e32 v98, v201
	v_mov_b32_e32 v99, v203
	v_cndmask_b32_e32 v17, v186, v17, vcc
	v_lshlrev_b32_e32 v17, 2, v17
	ds_bpermute_b32 v30, v17, v24
	ds_bpermute_b32 v31, v17, v25
	v_mov_b32_e32 v96, v200
	v_mov_b32_e32 v97, v202
	s_waitcnt lgkmcnt(0)
	v_pk_mul_f32 v[30:31], v[98:99], v[30:31]
	s_nop 0
	v_cndmask_b32_e64 v31, v31, -v31, s[4:5]
	v_cndmask_b32_e64 v30, v30, -v30, s[4:5]
	v_pk_fma_f32 v[24:25], v[24:25], v[96:97], v[30:31]
	ds_bpermute_b32 v30, v17, v22
	ds_bpermute_b32 v31, v17, v23
	v_mov_b32_e32 v98, v197
	v_mov_b32_e32 v99, v199
	v_mov_b32_e32 v96, v196
	v_mov_b32_e32 v97, v198
	s_waitcnt lgkmcnt(0)
	v_pk_mul_f32 v[30:31], v[98:99], v[30:31]
	v_mov_b32_e32 v98, v193
	v_cndmask_b32_e64 v31, v31, -v31, s[4:5]
	v_cndmask_b32_e64 v30, v30, -v30, s[4:5]
	v_pk_fma_f32 v[22:23], v[22:23], v[96:97], v[30:31]
	ds_bpermute_b32 v30, v17, v28
	ds_bpermute_b32 v31, v17, v29
	v_mov_b32_e32 v99, v195
	v_mov_b32_e32 v96, v192
	v_mov_b32_e32 v97, v194
	s_waitcnt lgkmcnt(0)
	v_pk_mul_f32 v[30:31], v[98:99], v[30:31]
	s_nop 0
	v_cndmask_b32_e64 v31, v31, -v31, s[4:5]
	v_cndmask_b32_e64 v30, v30, -v30, s[4:5]
	v_pk_fma_f32 v[28:29], v[28:29], v[96:97], v[30:31]
	ds_bpermute_b32 v30, v17, v26
	ds_bpermute_b32 v31, v17, v27
	v_mov_b32_e32 v98, v189
	v_mov_b32_e32 v99, v191
	v_mov_b32_e32 v96, v188
	v_mov_b32_e32 v97, v190
	s_waitcnt lgkmcnt(0)
	v_pk_mul_f32 v[30:31], v[98:99], v[30:31]
	s_nop 0
	v_cndmask_b32_e64 v31, v31, -v31, s[4:5]
	v_cndmask_b32_e64 v30, v30, -v30, s[4:5]
	v_pk_fma_f32 v[26:27], v[26:27], v[96:97], v[30:31]
	s_and_b64 vcc, exec, s[8:9]
	s_cbranch_vccz .LBB0_475

.LBB0_421:
	v_mul_lo_u32 v17, s75, v20
	v_mul_lo_u32 v30, s74, v21
	v_mad_u64_u32 v[20:21], s[30:31], s74, v20, 0
	v_add3_u32 v21, v21, v30, v17
	v_lshl_add_u64 v[20:21], v[20:21], 1, v[18:19]
	v_cvt_pk_bf16_f32 v88, v24, v25
	v_cvt_pk_bf16_f32 v89, v22, v23
	v_cvt_pk_bf16_f32 v90, v28, v29
	v_cvt_pk_bf16_f32 v91, v26, v27
	v_pk_mul_f32 v[22:23], v[86:87], s[48:49] op_sel_hi:[1,0]
	v_pk_mul_f32 v[24:25], v[84:85], s[48:49] op_sel_hi:[1,0]
	v_pk_mul_f32 v[26:27], v[82:83], s[48:49] op_sel_hi:[1,0]
	s_and_b64 vcc, exec, s[6:7]
	v_pk_mul_f32 v[28:29], v[80:81], s[48:49] op_sel_hi:[1,0]
	global_store_dwordx4 v[20:21], v[88:91], off
	s_cbranch_vccnz .LBB0_476
	v_and_b32_e32 v30, 64, v186
	v_xor_b32_e32 v17, 32, v186
	v_add_u32_e32 v30, 64, v30
	v_cmp_lt_i32_e32 vcc, v17, v30
	v_mov_b32_e32 v90, v201
	v_mov_b32_e32 v91, v203
	v_cndmask_b32_e32 v17, v186, v17, vcc
	v_lshlrev_b32_e32 v17, 2, v17
	ds_bpermute_b32 v30, v17, v24
	ds_bpermute_b32 v31, v17, v25
	v_mov_b32_e32 v88, v200
	v_mov_b32_e32 v89, v202
	s_waitcnt lgkmcnt(0)
	v_pk_mul_f32 v[30:31], v[90:91], v[30:31]
	s_nop 0
	v_cndmask_b32_e64 v31, v31, -v31, s[4:5]
	v_cndmask_b32_e64 v30, v30, -v30, s[4:5]
	v_pk_fma_f32 v[24:25], v[24:25], v[88:89], v[30:31]
	ds_bpermute_b32 v30, v17, v22
	ds_bpermute_b32 v31, v17, v23
	v_mov_b32_e32 v90, v197
	v_mov_b32_e32 v91, v199
	v_mov_b32_e32 v88, v196
	v_mov_b32_e32 v89, v198
	s_waitcnt lgkmcnt(0)
	v_pk_mul_f32 v[30:31], v[90:91], v[30:31]
	v_mov_b32_e32 v90, v193
	v_cndmask_b32_e64 v31, v31, -v31, s[4:5]
	v_cndmask_b32_e64 v30, v30, -v30, s[4:5]
	v_pk_fma_f32 v[22:23], v[22:23], v[88:89], v[30:31]
	ds_bpermute_b32 v30, v17, v28
	ds_bpermute_b32 v31, v17, v29
	v_mov_b32_e32 v91, v195
	v_mov_b32_e32 v88, v192
	v_mov_b32_e32 v89, v194
	s_waitcnt lgkmcnt(0)
	v_pk_mul_f32 v[30:31], v[90:91], v[30:31]
	s_nop 0
	v_cndmask_b32_e64 v31, v31, -v31, s[4:5]
	v_cndmask_b32_e64 v30, v30, -v30, s[4:5]
	v_pk_fma_f32 v[28:29], v[28:29], v[88:89], v[30:31]
	ds_bpermute_b32 v30, v17, v26
	ds_bpermute_b32 v31, v17, v27
	v_mov_b32_e32 v90, v189
	v_mov_b32_e32 v91, v191
	v_mov_b32_e32 v88, v188
	v_mov_b32_e32 v89, v190
	s_waitcnt lgkmcnt(0)
	v_pk_mul_f32 v[30:31], v[90:91], v[30:31]
	s_nop 0
	v_cndmask_b32_e64 v31, v31, -v31, s[4:5]
	v_cndmask_b32_e64 v30, v30, -v30, s[4:5]
	v_pk_fma_f32 v[26:27], v[26:27], v[88:89], v[30:31]
	s_and_b64 vcc, exec, s[8:9]
	s_cbranch_vccz .LBB0_477

.LBB0_427:
	v_pk_mul_f32 v[22:23], v[78:79], s[48:49] op_sel_hi:[1,0]
	v_pk_mul_f32 v[24:25], v[76:77], s[48:49] op_sel_hi:[1,0]
	v_pk_mul_f32 v[26:27], v[74:75], s[48:49] op_sel_hi:[1,0]
	s_and_b64 vcc, exec, s[6:7]
	v_pk_mul_f32 v[28:29], v[72:73], s[48:49] op_sel_hi:[1,0]
	s_cbranch_vccnz .LBB0_478
	v_and_b32_e32 v30, 64, v186
	v_xor_b32_e32 v17, 32, v186
	v_add_u32_e32 v30, 64, v30
	v_cmp_lt_i32_e32 vcc, v17, v30
	s_waitcnt vmcnt(14)
	v_mov_b32_e32 v82, v217
	v_mov_b32_e32 v83, v219
	v_cndmask_b32_e32 v17, v186, v17, vcc
	v_lshlrev_b32_e32 v17, 2, v17
	ds_bpermute_b32 v30, v17, v24
	ds_bpermute_b32 v31, v17, v25
	v_mov_b32_e32 v80, v216
	v_mov_b32_e32 v81, v218
	s_waitcnt lgkmcnt(0)
	v_pk_mul_f32 v[30:31], v[82:83], v[30:31]
	s_nop 0
	v_cndmask_b32_e64 v31, v31, -v31, s[4:5]
	v_cndmask_b32_e64 v30, v30, -v30, s[4:5]
	v_pk_fma_f32 v[24:25], v[24:25], v[80:81], v[30:31]
	ds_bpermute_b32 v30, v17, v22
	ds_bpermute_b32 v31, v17, v23
	v_mov_b32_e32 v82, v213
	v_mov_b32_e32 v83, v215
	v_mov_b32_e32 v80, v212
	v_mov_b32_e32 v81, v214
	s_waitcnt lgkmcnt(0)
	v_pk_mul_f32 v[30:31], v[82:83], v[30:31]
	v_mov_b32_e32 v82, v209
	v_cndmask_b32_e64 v31, v31, -v31, s[4:5]
	v_cndmask_b32_e64 v30, v30, -v30, s[4:5]
	v_pk_fma_f32 v[22:23], v[22:23], v[80:81], v[30:31]
	ds_bpermute_b32 v30, v17, v28
	ds_bpermute_b32 v31, v17, v29
	v_mov_b32_e32 v83, v211
	v_mov_b32_e32 v80, v208
	v_mov_b32_e32 v81, v210
	s_waitcnt lgkmcnt(0)
	v_pk_mul_f32 v[30:31], v[82:83], v[30:31]
	s_nop 0
	v_cndmask_b32_e64 v31, v31, -v31, s[4:5]
	v_cndmask_b32_e64 v30, v30, -v30, s[4:5]
	v_pk_fma_f32 v[28:29], v[28:29], v[80:81], v[30:31]
	ds_bpermute_b32 v30, v17, v26
	ds_bpermute_b32 v31, v17, v27
	v_mov_b32_e32 v82, v205
	v_mov_b32_e32 v83, v207
	v_mov_b32_e32 v80, v204
	v_mov_b32_e32 v81, v206
	s_waitcnt lgkmcnt(0)
	v_pk_mul_f32 v[30:31], v[82:83], v[30:31]
	s_nop 0
	v_cndmask_b32_e64 v31, v31, -v31, s[4:5]
	v_cndmask_b32_e64 v30, v30, -v30, s[4:5]
	v_pk_fma_f32 v[26:27], v[26:27], v[80:81], v[30:31]
	s_and_b64 vcc, exec, s[8:9]
	s_cbranch_vccz .LBB0_479

.LBB0_431:
	v_mul_lo_u32 v17, s75, v20
	v_mul_lo_u32 v30, s74, v21
	v_mad_u64_u32 v[20:21], s[30:31], s74, v20, 0
	v_add3_u32 v21, v21, v30, v17
	v_lshl_add_u64 v[20:21], v[20:21], 1, v[18:19]
	v_cvt_pk_bf16_f32 v72, v24, v25
	v_cvt_pk_bf16_f32 v73, v22, v23
	v_cvt_pk_bf16_f32 v74, v28, v29
	v_cvt_pk_bf16_f32 v75, v26, v27
	v_pk_mul_f32 v[22:23], v[70:71], s[48:49] op_sel_hi:[1,0]
	v_pk_mul_f32 v[24:25], v[68:69], s[48:49] op_sel_hi:[1,0]
	v_pk_mul_f32 v[26:27], v[66:67], s[48:49] op_sel_hi:[1,0]
	s_and_b64 vcc, exec, s[6:7]
	v_pk_mul_f32 v[28:29], v[64:65], s[48:49] op_sel_hi:[1,0]
	global_store_dwordx4 v[20:21], v[72:75], off
	s_cbranch_vccnz .LBB0_480
	v_and_b32_e32 v30, 64, v186
	v_xor_b32_e32 v17, 32, v186
	v_add_u32_e32 v30, 64, v30
	v_cmp_lt_i32_e32 vcc, v17, v30
	v_mov_b32_e32 v74, v217
	v_mov_b32_e32 v75, v219
	v_cndmask_b32_e32 v17, v186, v17, vcc
	v_lshlrev_b32_e32 v17, 2, v17
	ds_bpermute_b32 v30, v17, v24
	ds_bpermute_b32 v31, v17, v25
	v_mov_b32_e32 v72, v216
	v_mov_b32_e32 v73, v218
	s_waitcnt lgkmcnt(0)
	v_pk_mul_f32 v[30:31], v[74:75], v[30:31]
	s_nop 0
	v_cndmask_b32_e64 v31, v31, -v31, s[4:5]
	v_cndmask_b32_e64 v30, v30, -v30, s[4:5]
	v_pk_fma_f32 v[24:25], v[24:25], v[72:73], v[30:31]
	ds_bpermute_b32 v30, v17, v22
	ds_bpermute_b32 v31, v17, v23
	v_mov_b32_e32 v74, v213
	v_mov_b32_e32 v75, v215
	v_mov_b32_e32 v72, v212
	v_mov_b32_e32 v73, v214
	s_waitcnt lgkmcnt(0)
	v_pk_mul_f32 v[30:31], v[74:75], v[30:31]
	v_mov_b32_e32 v74, v209
	v_cndmask_b32_e64 v31, v31, -v31, s[4:5]
	v_cndmask_b32_e64 v30, v30, -v30, s[4:5]
	v_pk_fma_f32 v[22:23], v[22:23], v[72:73], v[30:31]
	ds_bpermute_b32 v30, v17, v28
	ds_bpermute_b32 v31, v17, v29
	v_mov_b32_e32 v75, v211
	v_mov_b32_e32 v72, v208
	v_mov_b32_e32 v73, v210
	s_waitcnt lgkmcnt(0)
	v_pk_mul_f32 v[30:31], v[74:75], v[30:31]
	s_nop 0
	v_cndmask_b32_e64 v31, v31, -v31, s[4:5]
	v_cndmask_b32_e64 v30, v30, -v30, s[4:5]
	v_pk_fma_f32 v[28:29], v[28:29], v[72:73], v[30:31]
	ds_bpermute_b32 v30, v17, v26
	ds_bpermute_b32 v31, v17, v27
	v_mov_b32_e32 v74, v205
	v_mov_b32_e32 v75, v207
	v_mov_b32_e32 v72, v204
	v_mov_b32_e32 v73, v206
	s_waitcnt lgkmcnt(0)
	v_pk_mul_f32 v[30:31], v[74:75], v[30:31]
	s_nop 0
	v_cndmask_b32_e64 v31, v31, -v31, s[4:5]
	v_cndmask_b32_e64 v30, v30, -v30, s[4:5]
	v_pk_fma_f32 v[26:27], v[26:27], v[72:73], v[30:31]
	s_and_b64 vcc, exec, s[8:9]
	s_cbranch_vccz .LBB0_481

.LBB0_437:
	v_pk_mul_f32 v[22:23], v[62:63], s[48:49] op_sel_hi:[1,0]
	v_pk_mul_f32 v[24:25], v[60:61], s[48:49] op_sel_hi:[1,0]
	v_pk_mul_f32 v[26:27], v[58:59], s[48:49] op_sel_hi:[1,0]
	s_and_b64 vcc, exec, s[6:7]
	v_pk_mul_f32 v[28:29], v[56:57], s[48:49] op_sel_hi:[1,0]
	s_cbranch_vccnz .LBB0_482
	v_and_b32_e32 v30, 64, v186
	v_xor_b32_e32 v17, 32, v186
	v_add_u32_e32 v30, 64, v30
	v_cmp_lt_i32_e32 vcc, v17, v30
	s_waitcnt vmcnt(10)
	v_mov_b32_e32 v66, v235
	v_mov_b32_e32 v67, v237
	v_cndmask_b32_e32 v17, v186, v17, vcc
	v_lshlrev_b32_e32 v17, 2, v17
	ds_bpermute_b32 v30, v17, v24
	ds_bpermute_b32 v31, v17, v25
	v_mov_b32_e32 v64, v234
	v_mov_b32_e32 v65, v236
	s_waitcnt lgkmcnt(0)
	v_pk_mul_f32 v[30:31], v[66:67], v[30:31]
	s_nop 0
	v_cndmask_b32_e64 v31, v31, -v31, s[4:5]
	v_cndmask_b32_e64 v30, v30, -v30, s[4:5]
	v_pk_fma_f32 v[24:25], v[24:25], v[64:65], v[30:31]
	ds_bpermute_b32 v30, v17, v22
	ds_bpermute_b32 v31, v17, v23
	v_mov_b32_e32 v66, v231
	v_mov_b32_e32 v67, v233
	v_mov_b32_e32 v64, v230
	v_mov_b32_e32 v65, v232
	s_waitcnt lgkmcnt(0)
	v_pk_mul_f32 v[30:31], v[66:67], v[30:31]
	v_mov_b32_e32 v66, v227
	v_cndmask_b32_e64 v31, v31, -v31, s[4:5]
	v_cndmask_b32_e64 v30, v30, -v30, s[4:5]
	v_pk_fma_f32 v[22:23], v[22:23], v[64:65], v[30:31]
	ds_bpermute_b32 v30, v17, v28
	ds_bpermute_b32 v31, v17, v29
	v_mov_b32_e32 v67, v229
	v_mov_b32_e32 v64, v226
	v_mov_b32_e32 v65, v228
	s_waitcnt lgkmcnt(0)
	v_pk_mul_f32 v[30:31], v[66:67], v[30:31]
	s_nop 0
	v_cndmask_b32_e64 v31, v31, -v31, s[4:5]
	v_cndmask_b32_e64 v30, v30, -v30, s[4:5]
	v_pk_fma_f32 v[28:29], v[28:29], v[64:65], v[30:31]
	ds_bpermute_b32 v30, v17, v26
	ds_bpermute_b32 v31, v17, v27
	v_mov_b32_e32 v66, v223
	v_mov_b32_e32 v67, v225
	v_mov_b32_e32 v64, v222
	v_mov_b32_e32 v65, v224
	s_waitcnt lgkmcnt(0)
	v_pk_mul_f32 v[30:31], v[66:67], v[30:31]
	s_nop 0
	v_cndmask_b32_e64 v31, v31, -v31, s[4:5]
	v_cndmask_b32_e64 v30, v30, -v30, s[4:5]
	v_pk_fma_f32 v[26:27], v[26:27], v[64:65], v[30:31]
	s_and_b64 vcc, exec, s[8:9]
	s_cbranch_vccz .LBB0_483

.LBB0_441:
	v_mul_lo_u32 v17, s75, v20
	v_mul_lo_u32 v30, s74, v21
	v_mad_u64_u32 v[20:21], s[30:31], s74, v20, 0
	v_add3_u32 v21, v21, v30, v17
	v_lshl_add_u64 v[20:21], v[20:21], 1, v[18:19]
	v_cvt_pk_bf16_f32 v56, v24, v25
	v_cvt_pk_bf16_f32 v57, v22, v23
	v_cvt_pk_bf16_f32 v58, v28, v29
	v_cvt_pk_bf16_f32 v59, v26, v27
	v_pk_mul_f32 v[22:23], v[54:55], s[48:49] op_sel_hi:[1,0]
	v_pk_mul_f32 v[24:25], v[52:53], s[48:49] op_sel_hi:[1,0]
	v_pk_mul_f32 v[26:27], v[50:51], s[48:49] op_sel_hi:[1,0]
	s_and_b64 vcc, exec, s[6:7]
	v_pk_mul_f32 v[28:29], v[48:49], s[48:49] op_sel_hi:[1,0]
	global_store_dwordx4 v[20:21], v[56:59], off
	s_cbranch_vccnz .LBB0_484
	v_and_b32_e32 v30, 64, v186
	v_xor_b32_e32 v17, 32, v186
	v_add_u32_e32 v30, 64, v30
	v_cmp_lt_i32_e32 vcc, v17, v30
	v_mov_b32_e32 v58, v235
	v_mov_b32_e32 v59, v237
	v_cndmask_b32_e32 v17, v186, v17, vcc
	v_lshlrev_b32_e32 v17, 2, v17
	ds_bpermute_b32 v30, v17, v24
	ds_bpermute_b32 v31, v17, v25
	v_mov_b32_e32 v56, v234
	v_mov_b32_e32 v57, v236
	s_waitcnt lgkmcnt(0)
	v_pk_mul_f32 v[30:31], v[58:59], v[30:31]
	s_nop 0
	v_cndmask_b32_e64 v31, v31, -v31, s[4:5]
	v_cndmask_b32_e64 v30, v30, -v30, s[4:5]
	v_pk_fma_f32 v[24:25], v[24:25], v[56:57], v[30:31]
	ds_bpermute_b32 v30, v17, v22
	ds_bpermute_b32 v31, v17, v23
	v_mov_b32_e32 v58, v231
	v_mov_b32_e32 v59, v233
	v_mov_b32_e32 v56, v230
	v_mov_b32_e32 v57, v232
	s_waitcnt lgkmcnt(0)
	v_pk_mul_f32 v[30:31], v[58:59], v[30:31]
	v_mov_b32_e32 v58, v227
	v_cndmask_b32_e64 v31, v31, -v31, s[4:5]
	v_cndmask_b32_e64 v30, v30, -v30, s[4:5]
	v_pk_fma_f32 v[22:23], v[22:23], v[56:57], v[30:31]
	ds_bpermute_b32 v30, v17, v28
	ds_bpermute_b32 v31, v17, v29
	v_mov_b32_e32 v59, v229
	v_mov_b32_e32 v56, v226
	v_mov_b32_e32 v57, v228
	s_waitcnt lgkmcnt(0)
	v_pk_mul_f32 v[30:31], v[58:59], v[30:31]
	s_nop 0
	v_cndmask_b32_e64 v31, v31, -v31, s[4:5]
	v_cndmask_b32_e64 v30, v30, -v30, s[4:5]
	v_pk_fma_f32 v[28:29], v[28:29], v[56:57], v[30:31]
	ds_bpermute_b32 v30, v17, v26
	ds_bpermute_b32 v31, v17, v27
	v_mov_b32_e32 v58, v223
	v_mov_b32_e32 v59, v225
	v_mov_b32_e32 v56, v222
	v_mov_b32_e32 v57, v224
	s_waitcnt lgkmcnt(0)
	v_pk_mul_f32 v[30:31], v[58:59], v[30:31]
	s_nop 0
	v_cndmask_b32_e64 v31, v31, -v31, s[4:5]
	v_cndmask_b32_e64 v30, v30, -v30, s[4:5]
	v_pk_fma_f32 v[26:27], v[26:27], v[56:57], v[30:31]
	s_and_b64 vcc, exec, s[8:9]
	s_cbranch_vccz .LBB0_485

.LBB0_447:
	v_pk_mul_f32 v[20:21], v[46:47], s[48:49] op_sel_hi:[1,0]
	v_pk_mul_f32 v[22:23], v[44:45], s[48:49] op_sel_hi:[1,0]
	v_pk_mul_f32 v[24:25], v[42:43], s[48:49] op_sel_hi:[1,0]
	s_and_b64 vcc, exec, s[6:7]
	v_pk_mul_f32 v[26:27], v[40:41], s[48:49] op_sel_hi:[1,0]
	s_cbranch_vccnz .LBB0_486
	v_and_b32_e32 v29, 64, v186
	v_xor_b32_e32 v28, 32, v186
	v_add_u32_e32 v29, 64, v29
	v_cmp_lt_i32_e32 vcc, v28, v29
	s_waitcnt vmcnt(6)
	v_mov_b32_e32 v48, v13
	v_mov_b32_e32 v49, v15
	v_cndmask_b32_e32 v28, v186, v28, vcc
	v_lshlrev_b32_e32 v50, 2, v28
	ds_bpermute_b32 v28, v50, v22
	ds_bpermute_b32 v29, v50, v23
	v_mov_b32_e32 v30, v12
	v_mov_b32_e32 v31, v14
	s_waitcnt lgkmcnt(0)
	v_pk_mul_f32 v[28:29], v[48:49], v[28:29]
	s_nop 0
	v_cndmask_b32_e64 v29, v29, -v29, s[4:5]
	v_cndmask_b32_e64 v28, v28, -v28, s[4:5]
	v_pk_fma_f32 v[22:23], v[22:23], v[30:31], v[28:29]
	ds_bpermute_b32 v28, v50, v20
	ds_bpermute_b32 v29, v50, v21
	v_mov_b32_e32 v48, v9
	v_mov_b32_e32 v49, v11
	v_mov_b32_e32 v30, v8
	v_mov_b32_e32 v31, v10
	s_waitcnt lgkmcnt(0)
	v_pk_mul_f32 v[28:29], v[48:49], v[28:29]
	v_mov_b32_e32 v48, v5
	v_cndmask_b32_e64 v29, v29, -v29, s[4:5]
	v_cndmask_b32_e64 v28, v28, -v28, s[4:5]
	v_pk_fma_f32 v[20:21], v[20:21], v[30:31], v[28:29]
	ds_bpermute_b32 v28, v50, v26
	ds_bpermute_b32 v29, v50, v27
	v_mov_b32_e32 v49, v7
	v_mov_b32_e32 v30, v4
	v_mov_b32_e32 v31, v6
	s_waitcnt lgkmcnt(0)
	v_pk_mul_f32 v[28:29], v[48:49], v[28:29]
	s_nop 0
	v_cndmask_b32_e64 v29, v29, -v29, s[4:5]
	v_cndmask_b32_e64 v28, v28, -v28, s[4:5]
	v_pk_fma_f32 v[26:27], v[26:27], v[30:31], v[28:29]
	ds_bpermute_b32 v28, v50, v24
	ds_bpermute_b32 v29, v50, v25
	v_mov_b32_e32 v48, v1
	v_mov_b32_e32 v49, v3
	v_mov_b32_e32 v30, v0
	v_mov_b32_e32 v31, v2
	s_waitcnt lgkmcnt(0)
	v_pk_mul_f32 v[28:29], v[48:49], v[28:29]
	s_nop 0
	v_cndmask_b32_e64 v29, v29, -v29, s[4:5]
	v_cndmask_b32_e64 v28, v28, -v28, s[4:5]
	v_pk_fma_f32 v[24:25], v[24:25], v[30:31], v[28:29]
	s_and_b64 vcc, exec, s[8:9]
	s_cbranch_vccz .LBB0_487

.LBB0_451:
	v_mul_lo_u32 v28, s75, v16
	v_mul_lo_u32 v29, s74, v17
	v_mad_u64_u32 v[16:17], s[30:31], s74, v16, 0
	v_add3_u32 v17, v17, v29, v28
	v_lshl_add_u64 v[16:17], v[16:17], 1, v[18:19]
	v_cvt_pk_bf16_f32 v18, v22, v23
	v_cvt_pk_bf16_f32 v19, v20, v21
	v_cvt_pk_bf16_f32 v20, v26, v27
	v_cvt_pk_bf16_f32 v21, v24, v25
	global_store_dwordx4 v[16:17], v[18:21], off
	v_pk_mul_f32 v[22:23], v[34:35], s[48:49] op_sel_hi:[1,0]
	s_and_b64 vcc, exec, s[6:7]
	v_pk_mul_f32 v[18:19], v[38:39], s[48:49] op_sel_hi:[1,0]
	v_pk_mul_f32 v[20:21], v[36:37], s[48:49] op_sel_hi:[1,0]
	v_pk_mul_f32 v[24:25], v[32:33], s[48:49] op_sel_hi:[1,0]
	s_cbranch_vccnz .LBB0_488
	v_and_b32_e32 v27, 64, v186
	v_xor_b32_e32 v26, 32, v186
	v_add_u32_e32 v27, 64, v27
	v_cmp_lt_i32_e32 vcc, v26, v27
	v_mov_b32_e32 v29, v14
	v_mov_b32_e32 v14, v13
	v_cndmask_b32_e32 v26, v186, v26, vcc
	v_lshlrev_b32_e32 v30, 2, v26
	ds_bpermute_b32 v26, v30, v20
	ds_bpermute_b32 v27, v30, v21
	v_mov_b32_e32 v28, v12
	s_waitcnt lgkmcnt(0)
	v_pk_mul_f32 v[12:13], v[14:15], v[26:27]
	ds_bpermute_b32 v14, v30, v18
	ds_bpermute_b32 v15, v30, v19
	v_cndmask_b32_e64 v13, v13, -v13, s[4:5]
	v_cndmask_b32_e64 v12, v12, -v12, s[4:5]
	v_pk_fma_f32 v[20:21], v[20:21], v[28:29], v[12:13]
	v_mov_b32_e32 v13, v10
	v_mov_b32_e32 v10, v9
	v_mov_b32_e32 v12, v8
	s_waitcnt lgkmcnt(0)
	v_pk_mul_f32 v[8:9], v[10:11], v[14:15]
	ds_bpermute_b32 v10, v30, v24
	ds_bpermute_b32 v11, v30, v25
	v_cndmask_b32_e64 v9, v9, -v9, s[4:5]
	v_cndmask_b32_e64 v8, v8, -v8, s[4:5]
	v_pk_fma_f32 v[18:19], v[18:19], v[12:13], v[8:9]
	v_mov_b32_e32 v9, v6
	v_mov_b32_e32 v6, v5
	v_mov_b32_e32 v8, v4
	s_waitcnt lgkmcnt(0)
	v_pk_mul_f32 v[4:5], v[6:7], v[10:11]
	ds_bpermute_b32 v6, v30, v22
	ds_bpermute_b32 v7, v30, v23
	v_cndmask_b32_e64 v5, v5, -v5, s[4:5]
	v_cndmask_b32_e64 v4, v4, -v4, s[4:5]
	v_pk_fma_f32 v[24:25], v[24:25], v[8:9], v[4:5]
	v_mov_b32_e32 v5, v2
	v_mov_b32_e32 v2, v1
	v_mov_b32_e32 v4, v0
	s_waitcnt lgkmcnt(0)
	v_pk_mul_f32 v[0:1], v[2:3], v[6:7]
	s_nop 0
	v_cndmask_b32_e64 v1, v1, -v1, s[4:5]
	v_cndmask_b32_e64 v0, v0, -v0, s[4:5]
	v_pk_fma_f32 v[22:23], v[22:23], v[4:5], v[0:1]
	s_and_b64 vcc, exec, s[8:9]
	s_cbranch_vccz .LBB0_489
